# v43 + NSA top-16 rank loop reads score[i] by v_readlane instead of ds_bpermute round trips
# baseline (speedup 1.0000x reference)
.LBB0_523:
	s_add_i32 s73, s72, s69
	v_lshl_add_u32 v51, s73, 8, v223
	ds_read2st64_b32 v[54:55], v51 offset1:32
	ds_read2st64_b32 v[56:57], v51 offset0:64 offset1:96
	v_mov_b32_e32 v53, 0
	v_mov_b32_e32 v51, v50
	s_mov_b32 s74, 0
	s_waitcnt lgkmcnt(1)
	v_add_f32_e32 v52, v54, v55
	s_waitcnt lgkmcnt(0)
	v_add_f32_e32 v54, v56, v57
	v_add_f32_e32 v52, v52, v54
	v_cndmask_b32_e64 v52, v52, v226, s[12:13]
	v_cndmask_b32_e32 v52, v52, v227, vcc
	s_nop 0
.LBB0_524:
	v_readlane_b32 s2, v52, s74
	v_cmp_lt_u32_e64 s[18:19], s74, v145
	s_nop 0
	v_cmp_eq_f32_e64 s[16:17], s2, v52
	v_cmp_gt_f32_e64 s[14:15], s2, v52
	s_and_b64 s[16:17], s[16:17], s[18:19]
	s_or_b64 s[14:15], s[14:15], s[16:17]
	v_addc_co_u32_e64 v53, s[14:15], 0, v53, s[14:15]
	s_add_i32 s74, s74, 1
	s_cmp_eq_u32 s74, 64
	s_cbranch_scc0 .LBB0_524
	v_cmp_gt_u32_e64 s[16:17], 16, v53
	s_and_saveexec_b64 s[14:15], s[10:11]
	s_cbranch_execz .LBB0_522
	s_lshl_b32 s2, s73, 3
	s_add_i32 s2, s2, 0
	s_add_i32 s2, s2, 0x18000
	v_mov_b32_e32 v51, s2
	v_mov_b64_e32 v[52:53], s[16:17]
	ds_write_b64 v51, v[52:53]
	s_branch .LBB0_522
